# output-slot LDS write deferred off the reduce path into the next node's layer-0 window; reduce waits split per partial read with b2 added early
# baseline (speedup 1.0000x reference)
.LBB1_2:
	v_lshrrev_b32_e32 v151, 4, v137
	s_lshl_b64 s[6:7], s[2:3], 4
	v_cmp_eq_u32_e64 s[2:3], 1, v151
	s_waitcnt vmcnt(31)
	v_cvt_f16_f32_e32 v8, v8
	v_cmp_gt_u32_e32 vcc, 16, v137
	s_waitcnt vmcnt(29)
	v_cndmask_b32_e64 v116, 0, v116, s[2:3]
	s_waitcnt vmcnt(21)
	v_cndmask_b32_e64 v100, 0, v100, s[2:3]
	v_cmp_eq_u32_e64 s[0:1], 2, v151
	v_cndmask_b32_e64 v114, 0, v114, s[2:3]
	v_cndmask_b32_e64 v115, 0, v115, s[2:3]
	v_cndmask_b32_e32 v6, v116, v6, vcc
	v_cndmask_b32_e64 v116, 0, v117, s[2:3]
	v_cndmask_b32_e64 v108, 0, v108, s[2:3]
	v_cndmask_b32_e32 v26, v100, v26, vcc
	v_cvt_f16_f32_e32 v29, v29
	v_cndmask_b32_e64 v100, 0, v101, s[2:3]
	v_cndmask_b32_e32 v28, 0, v28, vcc
	v_cndmask_b32_e64 v152, 0, 1.0, s[0:1]
	v_cndmask_b32_e32 v114, v114, v120, vcc
	v_cndmask_b32_e32 v115, v115, v121, vcc
	v_cndmask_b32_e32 v7, v116, v7, vcc
	v_cndmask_b32_e64 v106, 0, v106, s[2:3]
	v_cndmask_b32_e64 v107, 0, v107, s[2:3]
	v_cndmask_b32_e32 v14, v108, v14, vcc
	v_cndmask_b32_e64 v108, 0, v109, s[2:3]
	v_cndmask_b32_e32 v27, v100, v27, vcc
	v_cvt_f16_f32_e32 v100, v28
	v_cndmask_b32_e32 v116, 0, v8, vcc
	v_cvt_pk_f16_f32 v8, v6, v7
	v_cvt_pk_f16_f32 v7, v114, v115
	v_cndmask_b32_e64 v114, v152, v140, s[2:3]
	v_cndmask_b32_e32 v106, v106, v112, vcc
	v_cndmask_b32_e32 v107, v107, v113, vcc
	v_cndmask_b32_e32 v15, v108, v15, vcc
	v_cndmask_b32_e64 v98, 0, v98, s[2:3]
	v_cndmask_b32_e64 v99, 0, v99, s[2:3]
	v_cndmask_b32_e32 v110, v114, v110, vcc
	v_cndmask_b32_e64 v114, 0, v141, s[2:3]
	v_cndmask_b32_e32 v108, 0, v16, vcc
	v_cvt_pk_f16_f32 v16, v14, v15
	v_cvt_pk_f16_f32 v15, v106, v107
	v_cndmask_b32_e64 v106, v152, v138, s[2:3]
	v_cndmask_b32_e32 v98, v98, v104, vcc
	v_cndmask_b32_e32 v99, v99, v105, vcc
	v_cndmask_b32_e32 v111, v114, v111, vcc
	v_cndmask_b32_e32 v102, v106, v102, vcc
	v_cndmask_b32_e64 v106, 0, v139, s[2:3]
	v_cndmask_b32_e32 v29, 0, v29, vcc
	v_cvt_pk_f16_f32 v28, v26, v27
	v_cvt_pk_f16_f32 v27, v98, v99
	v_lshlrev_b32_e32 v101, 10, v1
	v_bitop3_b32 v98, v151, v0, 3 bitop3:0x78
	v_lshl_add_u64 v[130:131], s[4:5], 0, v[130:131]
	v_cvt_f16_f32_e32 v4, v4
	v_cvt_pk_f16_f32 v14, v110, v111
	v_cndmask_b32_e32 v103, v106, v103, vcc
	v_pack_b32_f16 v29, v100, v29
	v_lshl_or_b32 v111, v98, 4, v101
	v_lshlrev_b32_e32 v100, 4, v1
	s_movk_i32 s4, 0xc0
	v_cndmask_b32_e64 v124, 0, v124, s[2:3]
	v_cvt_pk_f16_f32 v26, v102, v103
	v_and_b32_e32 v112, 0xc0, v100
	v_bitop3_b32 v100, v100, s4, v111 bitop3:0x26
	s_lshl_b32 s4, s20, 3
	v_lshrrev_b32_e32 v102, 5, v137
	v_lshrrev_b32_e32 v104, 1, v137
	v_cndmask_b32_e64 v122, 0, v122, s[2:3]
	v_cndmask_b32_e64 v123, 0, v123, s[2:3]
	v_cndmask_b32_e32 v2, v124, v2, vcc
	v_cvt_f16_f32_e32 v5, v5
	v_cndmask_b32_e64 v124, 0, v125, s[2:3]
	v_cvt_f16_f32_e32 v9, v9
	v_or_b32_e32 v103, s4, v102
	v_and_or_b32 v110, v104, 8, v101
	v_bitop3_b32 v101, s4, v1, v102 bitop3:0x36
	s_lshl_b32 s4, s20, 4
	v_cndmask_b32_e32 v122, v122, v128, vcc
	v_cndmask_b32_e32 v123, v123, v129, vcc
	v_cndmask_b32_e32 v3, v124, v3, vcc
	v_cndmask_b32_e32 v17, 0, v17, vcc
	v_lshlrev_b32_e32 v107, 4, v101
	v_bitop3_b32 v101, v103, v1, 2 bitop3:0x36
	s_add_i32 s4, s4, 0x10000
	v_bfe_u32 v0, v0, 4, 2
	v_cndmask_b32_e64 v144, v152, v144, s[2:3]
	v_cndmask_b32_e32 v124, 0, v4, vcc
	v_cvt_pk_f16_f32 v4, v2, v3
	v_cvt_pk_f16_f32 v3, v122, v123
	v_cndmask_b32_e64 v122, v152, v142, s[2:3]
	v_cvt_pk_f16_f32 v17, v108, v17
	s_movk_i32 s5, 0x80
	v_lshlrev_b32_e32 v108, 4, v101
	v_bitop3_b32 v101, v103, v1, 4 bitop3:0x36
	s_cmp_lt_u32 s22, 64
	v_lshlrev_b32_e32 v104, 5, v0
	v_lshlrev_b32_e32 v0, 6, v0
	v_cndmask_b32_e32 v126, v144, v126, vcc
	v_cndmask_b32_e64 v144, 0, v145, s[2:3]
	v_cndmask_b32_e32 v118, v122, v118, vcc
	v_cndmask_b32_e64 v122, 0, v143, s[2:3]
	v_bitop3_b32 v99, v112, s5, v111 bitop3:0x36
	v_lshlrev_b32_e32 v109, 4, v101
	v_bitop3_b32 v101, v103, v1, 6 bitop3:0x36
	v_lshl_or_b32 v105, s20, 8, v0
	v_mov_b32_e32 v0, 0x1ec00
	s_cselect_b64 s[4:5], -1, 0
	v_cndmask_b32_e32 v127, v144, v127, vcc
	v_cndmask_b32_e32 v5, 0, v5, vcc
	v_cndmask_b32_e32 v119, v122, v119, vcc
	v_cndmask_b32_e32 v9, 0, v9, vcc
	v_lshlrev_b32_e32 v113, 4, v101
	v_lshlrev_b32_e32 v101, 5, v1
	v_lshl_add_u32 v106, v137, 6, v0
	s_cmp_eq_u32 s20, 0
	s_cselect_b32 s31, 0, 0xffff1d00
	v_add_u32_e32 v106, s31, v106
	v_cndmask_b32_e64 v0, 0, 1, s[4:5]
	v_lshl_add_u64 v[132:133], s[8:9], 0, v[132:133]
	v_or_b32_e32 v148, 0x400, v147
	v_or_b32_e32 v149, 0x800, v147
	v_or_b32_e32 v150, 0xc00, v147
	v_cvt_pk_f16_f32 v2, v126, v127
	v_pack_b32_f16 v5, v124, v5
	v_cvt_pk_f16_f32 v6, v118, v119
	v_pack_b32_f16 v9, v116, v9
	v_bitop3_b32 v98, v112, 64, v111 bitop3:0x36
	v_lshl_or_b32 v104, s20, 7, v104
	s_mov_b32 s22, 0x98000
	s_mov_b32 s23, 0x5040100
	s_mov_b32 s24, 0x7060302
	v_add_u32_e32 v107, v107, v110
	v_add_u32_e32 v108, v108, v110
	v_add_u32_e32 v109, v109, v110
	v_add_u32_e32 v110, v113, v110
	v_add_u32_e32 v111, v112, v111
	v_lshlrev_b32_e32 v113, 4, v137
	v_or_b32_e32 v113, 0x10000, v113
	s_lshr_b32 s28, s20, 2
	s_and_b32 s29, s20, 3
	s_lshl_b32 s28, s28, 10
	s_lshl_b32 s29, s29, 2
	s_add_i32 s28, s28, s29
	v_add_u32_e32 v112, s28, v113
	v_cmp_eq_u32_e64 s[26:27], 3, v151
	v_add_u32_e32 v114, 0x12400, v101
	v_mov_b32_e32 v121, v111
	v_mov_b32_e32 v144, v98
	v_cndmask_b32_e64 v111, v111, v99, s[84:85]
	v_cndmask_b32_e64 v99, v99, v121, s[84:85]
	v_cndmask_b32_e64 v98, v98, v100, s[84:85]
	v_cndmask_b32_e64 v100, v100, v144, s[84:85]
	v_add_u32_e32 v111, s80, v111
	v_add_u32_e32 v98, s81, v98
	v_add_u32_e32 v99, s82, v99
	v_add_u32_e32 v100, s83, v100
	v_and_b32_e32 v108, 15, v137
	s_lshl_b32 s31, s20, 3
	v_add_u32_e32 v107, s31, v151
	v_xor_b32_e32 v107, v107, v108
	v_lshlrev_b32_e32 v107, 4, v107
	v_lshl_or_b32 v107, v108, 10, v107
	v_xor_b32_e32 v108, 64, v107
	v_cmp_ne_u32_e64 s[4:5], 1, v0
	s_waitcnt vmcnt(16)
	v_cndmask_b32_e64 v1, v30, v134, s[0:1]
	v_bfi_b32 v30, s10, v1, v30
	v_perm_b32 v1, v22, v134, s24
	v_cndmask_b32_e64 v22, v22, v1, s[0:1]
	v_bfi_b32 v1, s10, v135, v18
	v_perm_b32 v121, v10, v135, s24
	v_cndmask_b32_e64 v18, v18, v1, s[0:1]
	v_cndmask_b32_e64 v10, v10, v121, s[0:1]
	v_mov_b32_e32 v121, v136
	v_mov_b32_e32 v144, v136
	v_mov_b32_e32 v145, v136
	v_mov_b32_e32 v0, v136
	v_mov_b32_e32 v1, v136
	s_waitcnt lgkmcnt(0)
	s_barrier
	ds_read_u16 v102, v114
	ds_read_u16 v103, v114 offset:512
	ds_read_u16 v115, v114 offset:1024
	ds_read_u16 v116, v114 offset:1536
	v_add_u32_e32 v0, 0x12c00, v105
	ds_read_b128 v[240:243], v0
	ds_read_b128 v[244:247], v0 offset:16
	ds_read_b128 v[248:251], v0 offset:32
	ds_read_b128 v[252:255], v0 offset:48
	v_add_u32_e32 v114, 2, v114
	s_waitcnt lgkmcnt(0)
	s_mov_b64 s[86:87], 0
	s_branch .LBB1_4
.LBB1_4:
	s_and_saveexec_b64 s[8:9], s[2:3]
	v_perm_b32 v5, v1, v102, s23
	v_perm_b32 v9, v121, v103, s23
	s_or_b64 exec, exec, s[8:9]
	v_mov_b32_e32 v144, v1
	v_mov_b32_e32 v145, v121
	v_mfma_f32_16x16x32_f16 v[164:167], v[30:33], v[2:5], 0
	v_mfma_f32_16x16x32_f16 v[180:183], v[22:25], v[2:5], 0
	s_cmp_lg_u32 s22, 0x818000
	v_permlane32_swap_b32_e32 v1, v144
	v_permlane32_swap_b32_e32 v121, v145
	v_mfma_f32_16x16x32_f16 v[168:171], v[30:33], v[6:9], 0
	v_mfma_f32_16x16x32_f16 v[184:187], v[22:25], v[6:9], 0
	s_cselect_b32 s9, s11, 15
	s_and_saveexec_b64 s[32:33], s[2:3]
	v_perm_b32 v17, v144, v115, s23
	v_perm_b32 v29, v145, v116, s23
	s_or_b64 exec, exec, s[32:33]
	v_mfma_f32_16x16x32_f16 v[172:175], v[30:33], v[14:17], 0
	v_mfma_f32_16x16x32_f16 v[188:191], v[22:25], v[14:17], 0
	v_mfma_f32_16x16x32_f16 v[176:179], v[30:33], v[26:29], 0
	v_mfma_f32_16x16x32_f16 v[192:195], v[22:25], v[26:29], 0
	v_mfma_f32_16x16x32_f16 v[208:211], v[18:21], v[2:5], 0
	v_mfma_f32_16x16x32_f16 v[224:227], v[10:13], v[2:5], 0
	v_cvt_pk_f16_f32 v122, v164, v165
	v_cvt_pk_f16_f32 v123, v166, v167
	v_pk_max_f16 v122, v122, 0
	v_pk_max_f16 v123, v123, 0
	v_cvt_pk_f16_f32 v124, v180, v181
	v_cvt_pk_f16_f32 v125, v182, v183
	v_pk_max_f16 v124, v124, 0
	v_pk_max_f16 v125, v125, 0
	ds_write_b128 v107, v[122:125]
	s_mov_b64 exec, s[86:87]
	ds_write_b32 v106, v0
	v_add_u32_e32 v106, 4, v106
	s_mov_b64 exec, -1
	v_mfma_f32_16x16x32_f16 v[212:215], v[18:21], v[6:9], 0
	v_mfma_f32_16x16x32_f16 v[228:231], v[10:13], v[6:9], 0
	v_cvt_pk_f16_f32 v126, v168, v169
	v_cvt_pk_f16_f32 v127, v170, v171
	v_pk_max_f16 v126, v126, 0
	v_pk_max_f16 v127, v127, 0
	v_cvt_pk_f16_f32 v128, v184, v185
	v_cvt_pk_f16_f32 v129, v186, v187
	v_pk_max_f16 v128, v128, 0
	v_pk_max_f16 v129, v129, 0
	ds_write_b128 v107, v[126:129] offset:16384
	v_mfma_f32_16x16x32_f16 v[216:219], v[18:21], v[14:17], 0
	v_mfma_f32_16x16x32_f16 v[232:235], v[10:13], v[14:17], 0
	v_cvt_pk_f16_f32 v134, v172, v173
	v_cvt_pk_f16_f32 v135, v174, v175
	v_pk_max_f16 v134, v134, 0
	v_pk_max_f16 v135, v135, 0
	v_cvt_pk_f16_f32 v136, v188, v189
	v_cvt_pk_f16_f32 v137, v190, v191
	v_pk_max_f16 v136, v136, 0
	v_pk_max_f16 v137, v137, 0
	ds_write_b128 v107, v[134:137] offset:32768
	v_mfma_f32_16x16x32_f16 v[220:223], v[18:21], v[26:29], 0
	v_mfma_f32_16x16x32_f16 v[236:239], v[10:13], v[26:29], 0
	v_cvt_pk_f16_f32 v138, v176, v177
	v_cvt_pk_f16_f32 v139, v178, v179
	v_pk_max_f16 v138, v138, 0
	v_pk_max_f16 v139, v139, 0
	v_cvt_pk_f16_f32 v140, v192, v193
	v_cvt_pk_f16_f32 v141, v194, v195
	v_pk_max_f16 v140, v140, 0
	v_pk_max_f16 v141, v141, 0
	ds_write_b128 v107, v[138:141] offset:49152
	v_add_u32_e32 v111, s64, v111
	v_add_u32_e32 v98, s65, v98
	s_lshl_b32 s20, s9, 7
	v_lshl_add_u64 v[0:1], s[20:21], 3, v[132:133]
	s_add_i32 s25, s22, s34
	s_lshl_b32 s8, s9, 8
	buffer_load_dwordx4 v[192:195], v147, s[16:19], s25 offen
	buffer_load_dwordx4 v[196:199], v148, s[16:19], s25 offen
	buffer_load_dwordx4 v[200:203], v149, s[16:19], s25 offen
	buffer_load_dwordx4 v[204:207], v150, s[16:19], s25 offen
	s_waitcnt vmcnt(19) lgkmcnt(5)
	v_mfma_f32_16x16x32_f16 v[164:167], v[58:61], v[122:125], v[240:243]
	s_load_dword s30, s[12:13], 0x0
	v_cvt_pk_f16_f32 v142, v208, v209
	v_cvt_pk_f16_f32 v143, v210, v211
	v_mfma_f32_16x16x32_f16 v[168:171], v[58:61], v[126:129], v[240:243]
	v_pk_max_f16 v142, v142, 0
	v_pk_max_f16 v143, v143, 0
	v_mfma_f32_16x16x32_f16 v[172:175], v[58:61], v[134:137], v[240:243]
	v_cvt_pk_f16_f32 v144, v224, v225
	v_cvt_pk_f16_f32 v145, v226, v227
	v_mfma_f32_16x16x32_f16 v[10:13], v[58:61], v[138:141], v[240:243]
	v_pk_max_f16 v144, v144, 0
	v_pk_max_f16 v145, v145, 0
	ds_write_b128 v108, v[142:145]
	s_waitcnt vmcnt(18)
	v_mfma_f32_16x16x32_f16 v[58:61], v[54:57], v[122:125], v[244:247]
	v_cvt_pk_f16_f32 v152, v212, v213
	v_cvt_pk_f16_f32 v153, v214, v215
	v_mfma_f32_16x16x32_f16 v[176:179], v[54:57], v[126:129], v[244:247]
	v_pk_max_f16 v152, v152, 0
	v_pk_max_f16 v153, v153, 0
	v_mfma_f32_16x16x32_f16 v[180:183], v[54:57], v[134:137], v[244:247]
	v_cvt_pk_f16_f32 v154, v228, v229
	v_cvt_pk_f16_f32 v155, v230, v231
	v_mfma_f32_16x16x32_f16 v[18:21], v[54:57], v[138:141], v[244:247]
	v_pk_max_f16 v154, v154, 0
	v_pk_max_f16 v155, v155, 0
	ds_write_b128 v108, v[152:155] offset:16384
	s_waitcnt vmcnt(17)
	v_mfma_f32_16x16x32_f16 v[54:57], v[50:53], v[122:125], v[248:251]
	v_cvt_pk_f16_f32 v156, v216, v217
	v_cvt_pk_f16_f32 v157, v218, v219
	v_mfma_f32_16x16x32_f16 v[184:187], v[50:53], v[126:129], v[248:251]
	v_pk_max_f16 v156, v156, 0
	v_pk_max_f16 v157, v157, 0
	v_mfma_f32_16x16x32_f16 v[188:191], v[50:53], v[134:137], v[248:251]
	v_cvt_pk_f16_f32 v158, v232, v233
	v_cvt_pk_f16_f32 v159, v234, v235
	v_mfma_f32_16x16x32_f16 v[22:25], v[50:53], v[138:141], v[248:251]
	v_pk_max_f16 v158, v158, 0
	v_pk_max_f16 v159, v159, 0
	ds_write_b128 v108, v[156:159] offset:32768
	s_waitcnt vmcnt(16)
	v_mfma_f32_16x16x32_f16 v[50:53], v[38:41], v[122:125], v[252:255]
	v_cvt_pk_f16_f32 v160, v220, v221
	v_cvt_pk_f16_f32 v161, v222, v223
	v_mfma_f32_16x16x32_f16 v[122:125], v[38:41], v[126:129], v[252:255]
	v_pk_max_f16 v160, v160, 0
	v_pk_max_f16 v161, v161, 0
	v_mfma_f32_16x16x32_f16 v[126:129], v[38:41], v[134:137], v[252:255]
	v_cvt_pk_f16_f32 v162, v236, v237
	v_cvt_pk_f16_f32 v163, v238, v239
	v_mfma_f32_16x16x32_f16 v[38:41], v[38:41], v[138:141], v[252:255]
	v_pk_max_f16 v162, v162, 0
	v_pk_max_f16 v163, v163, 0
	ds_write_b128 v108, v[160:163] offset:49152
	s_add_i32 s9, s22, s35
	s_waitcnt vmcnt(15)
	v_mfma_f32_16x16x32_f16 v[164:167], v[94:97], v[142:145], v[164:167]
	v_mfma_f32_16x16x32_f16 v[168:171], v[94:97], v[152:155], v[168:171]
	s_waitcnt vmcnt(14)
	v_mfma_f32_16x16x32_f16 v[58:61], v[90:93], v[142:145], v[58:61]
	v_mfma_f32_16x16x32_f16 v[176:179], v[90:93], v[152:155], v[176:179]
	s_waitcnt vmcnt(13)
	v_mfma_f32_16x16x32_f16 v[54:57], v[78:81], v[142:145], v[54:57]
	v_mfma_f32_16x16x32_f16 v[184:187], v[78:81], v[152:155], v[184:187]
	s_waitcnt vmcnt(12)
	v_mfma_f32_16x16x32_f16 v[50:53], v[34:37], v[142:145], v[50:53]
	buffer_load_dwordx4 v[140:143], v147, s[16:19], s9 offen
	buffer_load_dwordx4 v[220:223], v148, s[16:19], s9 offen
	v_mfma_f32_16x16x32_f16 v[122:125], v[34:37], v[152:155], v[122:125]
	buffer_load_dwordx4 v[152:155], v149, s[16:19], s9 offen
	buffer_load_dwordx4 v[224:227], v150, s[16:19], s9 offen
	s_mov_b32 s9, s21
	s_waitcnt lgkmcnt(0)
	s_barrier
	v_add_u32_e32 v99, s66, v99
	ds_read_b128 v[136:139], v99
	ds_read_b128 v[208:211], v99 offset:16384
	ds_read_b128 v[212:215], v99 offset:32768
	ds_read_b128 v[216:219], v99 offset:49152
	v_mfma_f32_16x16x32_f16 v[172:175], v[94:97], v[156:159], v[172:175]
	v_mfma_f32_16x16x32_f16 v[94:97], v[94:97], v[160:163], v[10:13]
	s_nop 2
	v_lshl_add_u64 v[10:11], s[8:9], 4, v[130:131]
	v_mfma_f32_16x16x32_f16 v[180:183], v[90:93], v[156:159], v[180:183]
	v_mfma_f32_16x16x32_f16 v[90:93], v[90:93], v[160:163], v[18:21]
	v_mfma_f32_16x16x32_f16 v[188:191], v[78:81], v[156:159], v[188:191]
	v_mfma_f32_16x16x32_f16 v[78:81], v[78:81], v[160:163], v[22:25]
	global_load_dwordx4 v[30:33], v[10:11], off
	s_nop 1
	global_load_dwordx4 v[22:25], v[10:11], off offset:1024
	global_load_dwordx4 v[18:21], v[10:11], off offset:2048
	s_nop 0
	global_load_dwordx4 v[10:13], v[10:11], off offset:3072
	s_nop 0
	global_load_dwordx2 v[134:135], v[0:1], off
	v_mfma_f32_16x16x32_f16 v[126:129], v[34:37], v[156:159], v[126:129]
	v_mfma_f32_16x16x32_f16 v[34:37], v[34:37], v[160:163], v[38:41]
	s_nop 2
	v_add_u32_e32 v100, s67, v100
	ds_read_b128 v[38:41], v100
	ds_read_b128 v[156:159], v100 offset:16384
	ds_read_b128 v[160:163], v100 offset:32768
	ds_read_b128 v[228:231], v100 offset:49152
	s_add_i32 s8, s22, s36
	s_waitcnt vmcnt(20) lgkmcnt(7)
	v_mfma_f32_16x16x32_f16 v[164:167], v[82:85], v[136:139], v[164:167]
	s_waitcnt lgkmcnt(6)
	v_mfma_f32_16x16x32_f16 v[168:171], v[82:85], v[208:211], v[168:171]
	s_waitcnt lgkmcnt(5)
	v_mfma_f32_16x16x32_f16 v[172:175], v[82:85], v[212:215], v[172:175]
	s_waitcnt lgkmcnt(4)
	v_mfma_f32_16x16x32_f16 v[82:85], v[82:85], v[216:219], v[94:97]
	s_waitcnt vmcnt(19)
	v_mfma_f32_16x16x32_f16 v[58:61], v[70:73], v[136:139], v[58:61]
	v_mfma_f32_16x16x32_f16 v[94:97], v[70:73], v[208:211], v[176:179]
	v_mfma_f32_16x16x32_f16 v[176:179], v[70:73], v[212:215], v[180:183]
	v_mfma_f32_16x16x32_f16 v[70:73], v[70:73], v[216:219], v[90:93]
	s_waitcnt vmcnt(18)
	v_mfma_f32_16x16x32_f16 v[54:57], v[62:65], v[136:139], v[54:57]
	v_mfma_f32_16x16x32_f16 v[90:93], v[62:65], v[208:211], v[184:187]
	v_mfma_f32_16x16x32_f16 v[180:183], v[62:65], v[212:215], v[188:191]
	v_mfma_f32_16x16x32_f16 v[62:65], v[62:65], v[216:219], v[78:81]
	s_waitcnt vmcnt(17)
	v_mfma_f32_16x16x32_f16 v[50:53], v[42:45], v[136:139], v[50:53]
	v_mfma_f32_16x16x32_f16 v[78:81], v[42:45], v[208:211], v[122:125]
	v_mfma_f32_16x16x32_f16 v[122:125], v[42:45], v[212:215], v[126:129]
	s_nop 2
	buffer_load_dwordx4 v[126:129], v147, s[16:19], s8 offen
	buffer_load_dwordx4 v[136:139], v148, s[16:19], s8 offen
	buffer_load_dwordx4 v[184:187], v149, s[16:19], s8 offen
	buffer_load_dwordx4 v[188:191], v150, s[16:19], s8 offen
	v_mfma_f32_16x16x32_f16 v[34:37], v[42:45], v[216:219], v[34:37]
	v_add_u32_e32 v111, s68, v111
	ds_read_b128 v[42:45], v111
	ds_read_b128 v[208:211], v111 offset:16384
	ds_read_b128 v[212:215], v111 offset:32768
	ds_read_b128 v[216:219], v111 offset:49152
	s_add_i32 s8, s22, s37
	s_waitcnt vmcnt(20) lgkmcnt(7)
	v_mfma_f32_16x16x32_f16 v[164:167], v[86:89], v[38:41], v[164:167]
	s_waitcnt lgkmcnt(6)
	v_mfma_f32_16x16x32_f16 v[168:171], v[86:89], v[156:159], v[168:171]
	s_waitcnt lgkmcnt(5)
	v_mfma_f32_16x16x32_f16 v[172:175], v[86:89], v[160:163], v[172:175]
	s_waitcnt lgkmcnt(4)
	v_mfma_f32_16x16x32_f16 v[82:85], v[86:89], v[228:231], v[82:85]
	s_waitcnt vmcnt(19)
	v_mfma_f32_16x16x32_f16 v[58:61], v[74:77], v[38:41], v[58:61]
	v_mfma_f32_16x16x32_f16 v[86:89], v[74:77], v[156:159], v[94:97]
	v_mfma_f32_16x16x32_f16 v[94:97], v[74:77], v[160:163], v[176:179]
	v_mfma_f32_16x16x32_f16 v[70:73], v[74:77], v[228:231], v[70:73]
	s_waitcnt vmcnt(18)
	v_mfma_f32_16x16x32_f16 v[54:57], v[66:69], v[38:41], v[54:57]
	v_mfma_f32_16x16x32_f16 v[74:77], v[66:69], v[156:159], v[90:93]
	v_mfma_f32_16x16x32_f16 v[90:93], v[66:69], v[160:163], v[180:183]
	v_mfma_f32_16x16x32_f16 v[62:65], v[66:69], v[228:231], v[62:65]
	s_waitcnt vmcnt(17)
	v_mfma_f32_16x16x32_f16 v[38:41], v[46:49], v[38:41], v[50:53]
	v_mfma_f32_16x16x32_f16 v[50:53], v[46:49], v[156:159], v[78:81]
	v_mfma_f32_16x16x32_f16 v[66:69], v[46:49], v[160:163], v[122:125]
	s_nop 1
	buffer_load_dwordx4 v[78:81], v147, s[16:19], s8 offen
	buffer_load_dwordx4 v[122:125], v148, s[16:19], s8 offen
	buffer_load_dwordx4 v[156:159], v149, s[16:19], s8 offen
	buffer_load_dwordx4 v[160:163], v150, s[16:19], s8 offen
	v_mfma_f32_16x16x32_f16 v[34:37], v[46:49], v[228:231], v[34:37]
	v_add_u32_e32 v98, s69, v98
	ds_read_b128 v[46:49], v98
	ds_read_b128 v[176:179], v98 offset:16384
	ds_read_b128 v[180:183], v98 offset:32768
	ds_read_b128 v[228:231], v98 offset:49152
	s_add_i32 s8, s22, s38
	s_waitcnt vmcnt(20) lgkmcnt(7)
	v_mfma_f32_16x16x32_f16 v[164:167], v[192:195], v[42:45], v[164:167]
	s_waitcnt lgkmcnt(6)
	v_mfma_f32_16x16x32_f16 v[168:171], v[192:195], v[208:211], v[168:171]
	s_waitcnt lgkmcnt(5)
	v_mfma_f32_16x16x32_f16 v[172:175], v[192:195], v[212:215], v[172:175]
	s_waitcnt lgkmcnt(4)
	v_mfma_f32_16x16x32_f16 v[82:85], v[192:195], v[216:219], v[82:85]
	s_waitcnt vmcnt(19)
	v_mfma_f32_16x16x32_f16 v[58:61], v[196:199], v[42:45], v[58:61]
	v_mfma_f32_16x16x32_f16 v[86:89], v[196:199], v[208:211], v[86:89]
	v_mfma_f32_16x16x32_f16 v[94:97], v[196:199], v[212:215], v[94:97]
	v_mfma_f32_16x16x32_f16 v[70:73], v[196:199], v[216:219], v[70:73]
	s_waitcnt vmcnt(18)
	v_mfma_f32_16x16x32_f16 v[54:57], v[200:203], v[42:45], v[54:57]
	v_mfma_f32_16x16x32_f16 v[74:77], v[200:203], v[208:211], v[74:77]
	v_mfma_f32_16x16x32_f16 v[90:93], v[200:203], v[212:215], v[90:93]
	v_mfma_f32_16x16x32_f16 v[62:65], v[200:203], v[216:219], v[62:65]
	s_waitcnt vmcnt(17)
	v_mfma_f32_16x16x32_f16 v[38:41], v[204:207], v[42:45], v[38:41]
	v_mfma_f32_16x16x32_f16 v[42:45], v[204:207], v[208:211], v[50:53]
	v_mfma_f32_16x16x32_f16 v[50:53], v[204:207], v[212:215], v[66:69]
	s_nop 2
	buffer_load_dwordx4 v[66:69], v147, s[16:19], s8 offen
	buffer_load_dwordx4 v[192:195], v148, s[16:19], s8 offen
	buffer_load_dwordx4 v[196:199], v149, s[16:19], s8 offen
	buffer_load_dwordx4 v[200:203], v150, s[16:19], s8 offen
	v_mfma_f32_16x16x32_f16 v[34:37], v[204:207], v[216:219], v[34:37]
	v_add_u32_e32 v99, s70, v99
	ds_read_b128 v[204:207], v99
	ds_read_b128 v[208:211], v99 offset:16384
	ds_read_b128 v[212:215], v99 offset:32768
	ds_read_b128 v[216:219], v99 offset:49152
	s_add_i32 s8, s22, s39
	s_waitcnt vmcnt(20) lgkmcnt(7)
	v_mfma_f32_16x16x32_f16 v[164:167], v[140:143], v[46:49], v[164:167]
	s_waitcnt lgkmcnt(6)
	v_mfma_f32_16x16x32_f16 v[168:171], v[140:143], v[176:179], v[168:171]
	s_waitcnt lgkmcnt(5)
	v_mfma_f32_16x16x32_f16 v[172:175], v[140:143], v[180:183], v[172:175]
	s_waitcnt lgkmcnt(4)
	v_mfma_f32_16x16x32_f16 v[82:85], v[140:143], v[228:231], v[82:85]
	s_waitcnt vmcnt(19)
	v_mfma_f32_16x16x32_f16 v[58:61], v[220:223], v[46:49], v[58:61]
	v_mfma_f32_16x16x32_f16 v[86:89], v[220:223], v[176:179], v[86:89]
	s_waitcnt vmcnt(18)
	v_mfma_f32_16x16x32_f16 v[54:57], v[152:155], v[46:49], v[54:57]
	v_mfma_f32_16x16x32_f16 v[74:77], v[152:155], v[176:179], v[74:77]
	v_mfma_f32_16x16x32_f16 v[90:93], v[152:155], v[180:183], v[90:93]
	v_mfma_f32_16x16x32_f16 v[62:65], v[152:155], v[228:231], v[62:65]
	s_waitcnt vmcnt(17)
	v_mfma_f32_16x16x32_f16 v[38:41], v[224:227], v[46:49], v[38:41]
	v_mfma_f32_16x16x32_f16 v[42:45], v[224:227], v[176:179], v[42:45]
	v_mfma_f32_16x16x32_f16 v[46:49], v[224:227], v[180:183], v[50:53]
	s_nop 2
	buffer_load_dwordx4 v[50:53], v147, s[16:19], s8 offen
	buffer_load_dwordx4 v[140:143], v148, s[16:19], s8 offen
	buffer_load_dwordx4 v[152:155], v149, s[16:19], s8 offen
	buffer_load_dwordx4 v[176:179], v150, s[16:19], s8 offen
	v_mfma_f32_16x16x32_f16 v[94:97], v[220:223], v[180:183], v[94:97]
	v_mfma_f32_16x16x32_f16 v[70:73], v[220:223], v[228:231], v[70:73]
	v_mfma_f32_16x16x32_f16 v[34:37], v[224:227], v[228:231], v[34:37]
	v_add_u32_e32 v100, s71, v100
	ds_read_b128 v[180:183], v100
	ds_read_b128 v[220:223], v100 offset:16384
	ds_read_b128 v[224:227], v100 offset:32768
	ds_read_b128 v[228:231], v100 offset:49152
	s_add_i32 s8, s22, s40
	s_waitcnt vmcnt(15) lgkmcnt(7)
	v_mfma_f32_16x16x32_f16 v[164:167], v[126:129], v[204:207], v[164:167]
	s_waitcnt lgkmcnt(6)
	v_mfma_f32_16x16x32_f16 v[168:171], v[126:129], v[208:211], v[168:171]
	s_waitcnt lgkmcnt(5)
	v_mfma_f32_16x16x32_f16 v[172:175], v[126:129], v[212:215], v[172:175]
	s_waitcnt lgkmcnt(4)
	v_mfma_f32_16x16x32_f16 v[82:85], v[126:129], v[216:219], v[82:85]
	s_waitcnt vmcnt(14)
	v_mfma_f32_16x16x32_f16 v[58:61], v[136:139], v[204:207], v[58:61]
	v_mfma_f32_16x16x32_f16 v[86:89], v[136:139], v[208:211], v[86:89]
	v_mfma_f32_16x16x32_f16 v[94:97], v[136:139], v[212:215], v[94:97]
	v_mfma_f32_16x16x32_f16 v[70:73], v[136:139], v[216:219], v[70:73]
	s_waitcnt vmcnt(13)
	v_mfma_f32_16x16x32_f16 v[54:57], v[184:187], v[204:207], v[54:57]
	v_mfma_f32_16x16x32_f16 v[74:77], v[184:187], v[208:211], v[74:77]
	v_mfma_f32_16x16x32_f16 v[90:93], v[184:187], v[212:215], v[90:93]
	v_mfma_f32_16x16x32_f16 v[62:65], v[184:187], v[216:219], v[62:65]
	s_waitcnt vmcnt(12)
	v_mfma_f32_16x16x32_f16 v[38:41], v[188:191], v[204:207], v[38:41]
	buffer_load_dwordx4 v[126:129], v147, s[16:19], s8 offen
	buffer_load_dwordx4 v[136:139], v148, s[16:19], s8 offen
	buffer_load_dwordx4 v[184:187], v149, s[16:19], s8 offen
	buffer_load_dwordx4 v[204:207], v150, s[16:19], s8 offen
	v_mfma_f32_16x16x32_f16 v[42:45], v[188:191], v[208:211], v[42:45]
	v_mfma_f32_16x16x32_f16 v[46:49], v[188:191], v[212:215], v[46:49]
	v_mfma_f32_16x16x32_f16 v[34:37], v[188:191], v[216:219], v[34:37]
	v_add_u32_e32 v111, s72, v111
	ds_read_b128 v[188:191], v111
	ds_read_b128 v[208:211], v111 offset:16384
	ds_read_b128 v[212:215], v111 offset:32768
	ds_read_b128 v[216:219], v111 offset:49152
	s_add_i32 s8, s22, s41
	s_waitcnt vmcnt(15) lgkmcnt(7)
	v_mfma_f32_16x16x32_f16 v[164:167], v[78:81], v[180:183], v[164:167]
	s_waitcnt lgkmcnt(6)
	v_mfma_f32_16x16x32_f16 v[168:171], v[78:81], v[220:223], v[168:171]
	s_waitcnt lgkmcnt(5)
	v_mfma_f32_16x16x32_f16 v[172:175], v[78:81], v[224:227], v[172:175]
	s_waitcnt lgkmcnt(4)
	v_mfma_f32_16x16x32_f16 v[78:81], v[78:81], v[228:231], v[82:85]
	s_waitcnt vmcnt(14)
	v_mfma_f32_16x16x32_f16 v[58:61], v[122:125], v[180:183], v[58:61]
	v_mfma_f32_16x16x32_f16 v[82:85], v[122:125], v[220:223], v[86:89]
	v_mfma_f32_16x16x32_f16 v[86:89], v[122:125], v[224:227], v[94:97]
	v_mfma_f32_16x16x32_f16 v[70:73], v[122:125], v[228:231], v[70:73]
	s_waitcnt vmcnt(13)
	v_mfma_f32_16x16x32_f16 v[54:57], v[156:159], v[180:183], v[54:57]
	v_mfma_f32_16x16x32_f16 v[74:77], v[156:159], v[220:223], v[74:77]
	v_mfma_f32_16x16x32_f16 v[90:93], v[156:159], v[224:227], v[90:93]
	v_mfma_f32_16x16x32_f16 v[62:65], v[156:159], v[228:231], v[62:65]
	s_waitcnt vmcnt(12)
	v_mfma_f32_16x16x32_f16 v[38:41], v[160:163], v[180:183], v[38:41]
	buffer_load_dwordx4 v[94:97], v147, s[16:19], s8 offen
	buffer_load_dwordx4 v[122:125], v148, s[16:19], s8 offen
	buffer_load_dwordx4 v[156:159], v149, s[16:19], s8 offen
	buffer_load_dwordx4 v[180:183], v150, s[16:19], s8 offen
	v_mfma_f32_16x16x32_f16 v[42:45], v[160:163], v[220:223], v[42:45]
	v_mfma_f32_16x16x32_f16 v[46:49], v[160:163], v[224:227], v[46:49]
	v_mfma_f32_16x16x32_f16 v[34:37], v[160:163], v[228:231], v[34:37]
	v_add_u32_e32 v98, s73, v98
	ds_read_b128 v[160:163], v98
	ds_read_b128 v[220:223], v98 offset:16384
	ds_read_b128 v[224:227], v98 offset:32768
	ds_read_b128 v[228:231], v98 offset:49152
	s_add_i32 s8, s22, s42
	s_waitcnt vmcnt(15) lgkmcnt(7)
	v_mfma_f32_16x16x32_f16 v[164:167], v[66:69], v[188:191], v[164:167]
	s_waitcnt lgkmcnt(6)
	v_mfma_f32_16x16x32_f16 v[168:171], v[66:69], v[208:211], v[168:171]
	s_waitcnt lgkmcnt(5)
	v_mfma_f32_16x16x32_f16 v[172:175], v[66:69], v[212:215], v[172:175]
	s_waitcnt lgkmcnt(4)
	v_mfma_f32_16x16x32_f16 v[66:69], v[66:69], v[216:219], v[78:81]
	s_waitcnt vmcnt(14)
	v_mfma_f32_16x16x32_f16 v[58:61], v[192:195], v[188:191], v[58:61]
	v_mfma_f32_16x16x32_f16 v[78:81], v[192:195], v[208:211], v[82:85]
	v_mfma_f32_16x16x32_f16 v[82:85], v[192:195], v[212:215], v[86:89]
	v_mfma_f32_16x16x32_f16 v[70:73], v[192:195], v[216:219], v[70:73]
	s_waitcnt vmcnt(13)
	v_mfma_f32_16x16x32_f16 v[54:57], v[196:199], v[188:191], v[54:57]
	v_mfma_f32_16x16x32_f16 v[74:77], v[196:199], v[208:211], v[74:77]
	v_mfma_f32_16x16x32_f16 v[86:89], v[196:199], v[212:215], v[90:93]
	v_mfma_f32_16x16x32_f16 v[62:65], v[196:199], v[216:219], v[62:65]
	s_waitcnt vmcnt(12)
	v_mfma_f32_16x16x32_f16 v[38:41], v[200:203], v[188:191], v[38:41]
	buffer_load_dwordx4 v[90:93], v147, s[16:19], s8 offen
	buffer_load_dwordx4 v[188:191], v148, s[16:19], s8 offen
	buffer_load_dwordx4 v[192:195], v149, s[16:19], s8 offen
	buffer_load_dwordx4 v[196:199], v150, s[16:19], s8 offen
	v_mfma_f32_16x16x32_f16 v[42:45], v[200:203], v[208:211], v[42:45]
	v_mfma_f32_16x16x32_f16 v[46:49], v[200:203], v[212:215], v[46:49]
	v_mfma_f32_16x16x32_f16 v[34:37], v[200:203], v[216:219], v[34:37]
	v_add_u32_e32 v99, s74, v99
	ds_read_b128 v[200:203], v99
	ds_read_b128 v[208:211], v99 offset:16384
	ds_read_b128 v[212:215], v99 offset:32768
	ds_read_b128 v[216:219], v99 offset:49152
	s_add_i32 s8, s22, s43
	s_waitcnt vmcnt(15) lgkmcnt(7)
	v_mfma_f32_16x16x32_f16 v[164:167], v[50:53], v[160:163], v[164:167]
	s_waitcnt lgkmcnt(6)
	v_mfma_f32_16x16x32_f16 v[168:171], v[50:53], v[220:223], v[168:171]
	s_waitcnt lgkmcnt(5)
	v_mfma_f32_16x16x32_f16 v[172:175], v[50:53], v[224:227], v[172:175]
	s_waitcnt lgkmcnt(4)
	v_mfma_f32_16x16x32_f16 v[50:53], v[50:53], v[228:231], v[66:69]
	s_waitcnt vmcnt(14)
	v_mfma_f32_16x16x32_f16 v[58:61], v[140:143], v[160:163], v[58:61]
	v_mfma_f32_16x16x32_f16 v[66:69], v[140:143], v[220:223], v[78:81]
	v_mfma_f32_16x16x32_f16 v[78:81], v[140:143], v[224:227], v[82:85]
	v_mfma_f32_16x16x32_f16 v[70:73], v[140:143], v[228:231], v[70:73]
	s_waitcnt vmcnt(13)
	v_mfma_f32_16x16x32_f16 v[54:57], v[152:155], v[160:163], v[54:57]
	v_mfma_f32_16x16x32_f16 v[74:77], v[152:155], v[220:223], v[74:77]
	v_mfma_f32_16x16x32_f16 v[82:85], v[152:155], v[224:227], v[86:89]
	v_mfma_f32_16x16x32_f16 v[62:65], v[152:155], v[228:231], v[62:65]
	s_waitcnt vmcnt(12)
	v_mfma_f32_16x16x32_f16 v[38:41], v[176:179], v[160:163], v[38:41]
	buffer_load_dwordx4 v[86:89], v147, s[16:19], s8 offen
	buffer_load_dwordx4 v[140:143], v148, s[16:19], s8 offen
	buffer_load_dwordx4 v[152:155], v149, s[16:19], s8 offen
	buffer_load_dwordx4 v[160:163], v150, s[16:19], s8 offen
	v_mfma_f32_16x16x32_f16 v[42:45], v[176:179], v[220:223], v[42:45]
	v_mfma_f32_16x16x32_f16 v[46:49], v[176:179], v[224:227], v[46:49]
	v_mfma_f32_16x16x32_f16 v[34:37], v[176:179], v[228:231], v[34:37]
	v_add_u32_e32 v100, s75, v100
	ds_read_b128 v[176:179], v100
	ds_read_b128 v[220:223], v100 offset:16384
	ds_read_b128 v[224:227], v100 offset:32768
	ds_read_b128 v[228:231], v100 offset:49152
	s_add_i32 s8, s22, s44
	s_waitcnt vmcnt(15) lgkmcnt(7)
	v_mfma_f32_16x16x32_f16 v[164:167], v[126:129], v[200:203], v[164:167]
	s_waitcnt lgkmcnt(6)
	v_mfma_f32_16x16x32_f16 v[168:171], v[126:129], v[208:211], v[168:171]
	s_waitcnt lgkmcnt(5)
	v_mfma_f32_16x16x32_f16 v[172:175], v[126:129], v[212:215], v[172:175]
	s_waitcnt lgkmcnt(4)
	v_mfma_f32_16x16x32_f16 v[50:53], v[126:129], v[216:219], v[50:53]
	s_waitcnt vmcnt(14)
	v_mfma_f32_16x16x32_f16 v[58:61], v[136:139], v[200:203], v[58:61]
	v_mfma_f32_16x16x32_f16 v[66:69], v[136:139], v[208:211], v[66:69]
	v_mfma_f32_16x16x32_f16 v[78:81], v[136:139], v[212:215], v[78:81]
	v_mfma_f32_16x16x32_f16 v[70:73], v[136:139], v[216:219], v[70:73]
	s_waitcnt vmcnt(13)
	v_mfma_f32_16x16x32_f16 v[54:57], v[184:187], v[200:203], v[54:57]
	v_mfma_f32_16x16x32_f16 v[74:77], v[184:187], v[208:211], v[74:77]
	v_mfma_f32_16x16x32_f16 v[82:85], v[184:187], v[212:215], v[82:85]
	v_mfma_f32_16x16x32_f16 v[62:65], v[184:187], v[216:219], v[62:65]
	s_waitcnt vmcnt(12)
	v_mfma_f32_16x16x32_f16 v[38:41], v[204:207], v[200:203], v[38:41]
	buffer_load_dwordx4 v[126:129], v147, s[16:19], s8 offen
	buffer_load_dwordx4 v[136:139], v148, s[16:19], s8 offen
	buffer_load_dwordx4 v[184:187], v149, s[16:19], s8 offen
	buffer_load_dwordx4 v[200:203], v150, s[16:19], s8 offen
	v_mfma_f32_16x16x32_f16 v[42:45], v[204:207], v[208:211], v[42:45]
	v_mfma_f32_16x16x32_f16 v[46:49], v[204:207], v[212:215], v[46:49]
	v_mfma_f32_16x16x32_f16 v[34:37], v[204:207], v[216:219], v[34:37]
	v_add_u32_e32 v111, s76, v111
	ds_read_b128 v[204:207], v111
	ds_read_b128 v[208:211], v111 offset:16384
	ds_read_b128 v[212:215], v111 offset:32768
	ds_read_b128 v[216:219], v111 offset:49152
	s_add_i32 s8, s22, s45
	s_waitcnt vmcnt(15) lgkmcnt(7)
	v_mfma_f32_16x16x32_f16 v[164:167], v[94:97], v[176:179], v[164:167]
	s_waitcnt lgkmcnt(6)
	v_mfma_f32_16x16x32_f16 v[168:171], v[94:97], v[220:223], v[168:171]
	s_waitcnt vmcnt(14)
	v_mfma_f32_16x16x32_f16 v[58:61], v[122:125], v[176:179], v[58:61]
	v_mfma_f32_16x16x32_f16 v[66:69], v[122:125], v[220:223], v[66:69]
	s_waitcnt lgkmcnt(5)
	v_mfma_f32_16x16x32_f16 v[78:81], v[122:125], v[224:227], v[78:81]
	s_waitcnt lgkmcnt(4)
	v_mfma_f32_16x16x32_f16 v[70:73], v[122:125], v[228:231], v[70:73]
	s_waitcnt vmcnt(13)
	v_mfma_f32_16x16x32_f16 v[54:57], v[156:159], v[176:179], v[54:57]
	v_mfma_f32_16x16x32_f16 v[74:77], v[156:159], v[220:223], v[74:77]
	v_mfma_f32_16x16x32_f16 v[82:85], v[156:159], v[224:227], v[82:85]
	v_mfma_f32_16x16x32_f16 v[62:65], v[156:159], v[228:231], v[62:65]
	s_waitcnt vmcnt(12)
	v_mfma_f32_16x16x32_f16 v[38:41], v[180:183], v[176:179], v[38:41]
	v_mfma_f32_16x16x32_f16 v[42:45], v[180:183], v[220:223], v[42:45]
	buffer_load_dwordx4 v[122:125], v147, s[16:19], s8 offen
	buffer_load_dwordx4 v[156:159], v148, s[16:19], s8 offen
	buffer_load_dwordx4 v[176:179], v149, s[16:19], s8 offen
	buffer_load_dwordx4 v[220:223], v150, s[16:19], s8 offen
	v_mfma_f32_16x16x32_f16 v[50:53], v[94:97], v[228:231], v[50:53]
	v_mfma_f32_16x16x32_f16 v[46:49], v[180:183], v[224:227], v[46:49]
	v_mfma_f32_16x16x32_f16 v[34:37], v[180:183], v[228:231], v[34:37]
	v_mfma_f32_16x16x32_f16 v[172:175], v[94:97], v[224:227], v[172:175]
	v_add_u32_e32 v98, s77, v98
	ds_read_b128 v[94:97], v98
	ds_read_b128 v[180:183], v98 offset:16384
	ds_read_b128 v[224:227], v98 offset:32768
	ds_read_b128 v[228:231], v98 offset:49152
	s_add_i32 s8, s22, s46
	s_waitcnt vmcnt(15) lgkmcnt(7)
	v_mfma_f32_16x16x32_f16 v[164:167], v[90:93], v[204:207], v[164:167]
	s_waitcnt lgkmcnt(6)
	v_mfma_f32_16x16x32_f16 v[168:171], v[90:93], v[208:211], v[168:171]
	s_waitcnt lgkmcnt(5)
	v_mfma_f32_16x16x32_f16 v[172:175], v[90:93], v[212:215], v[172:175]
	s_waitcnt lgkmcnt(4)
	v_mfma_f32_16x16x32_f16 v[90:93], v[90:93], v[216:219], v[50:53]
	s_waitcnt vmcnt(14)
	v_mfma_f32_16x16x32_f16 v[232:235], v[188:191], v[204:207], v[58:61]
	v_mfma_f32_16x16x32_f16 v[66:69], v[188:191], v[208:211], v[66:69]
	v_mfma_f32_16x16x32_f16 v[78:81], v[188:191], v[212:215], v[78:81]
	v_mfma_f32_16x16x32_f16 v[70:73], v[188:191], v[216:219], v[70:73]
	s_waitcnt vmcnt(13)
	v_mfma_f32_16x16x32_f16 v[188:191], v[192:195], v[204:207], v[54:57]
	v_mfma_f32_16x16x32_f16 v[74:77], v[192:195], v[208:211], v[74:77]
	v_mfma_f32_16x16x32_f16 v[82:85], v[192:195], v[212:215], v[82:85]
	v_mfma_f32_16x16x32_f16 v[62:65], v[192:195], v[216:219], v[62:65]
	s_waitcnt vmcnt(12)
	v_mfma_f32_16x16x32_f16 v[192:195], v[196:199], v[204:207], v[38:41]
	buffer_load_dwordx4 v[58:61], v147, s[16:19], s8 offen
	buffer_load_dwordx4 v[54:57], v148, s[16:19], s8 offen
	buffer_load_dwordx4 v[50:53], v149, s[16:19], s8 offen
	buffer_load_dwordx4 v[38:41], v150, s[16:19], s8 offen
	v_mfma_f32_16x16x32_f16 v[42:45], v[196:199], v[208:211], v[42:45]
	v_mfma_f32_16x16x32_f16 v[46:49], v[196:199], v[212:215], v[46:49]
	v_mfma_f32_16x16x32_f16 v[196:199], v[196:199], v[216:219], v[34:37]
	v_add_u32_e32 v99, s78, v99
	ds_read_b128 v[204:207], v99
	ds_read_b128 v[208:211], v99 offset:16384
	ds_read_b128 v[212:215], v99 offset:32768
	ds_read_b128 v[216:219], v99 offset:49152
	s_add_i32 s8, s22, s47
	s_waitcnt vmcnt(15) lgkmcnt(7)
	v_mfma_f32_16x16x32_f16 v[164:167], v[86:89], v[94:97], v[164:167]
	s_waitcnt lgkmcnt(6)
	v_mfma_f32_16x16x32_f16 v[168:171], v[86:89], v[180:183], v[168:171]
	s_waitcnt lgkmcnt(5)
	v_mfma_f32_16x16x32_f16 v[172:175], v[86:89], v[224:227], v[172:175]
	s_waitcnt lgkmcnt(4)
	v_mfma_f32_16x16x32_f16 v[86:89], v[86:89], v[228:231], v[90:93]
	s_waitcnt vmcnt(14)
	v_mfma_f32_16x16x32_f16 v[232:235], v[140:143], v[94:97], v[232:235]
	v_mfma_f32_16x16x32_f16 v[66:69], v[140:143], v[180:183], v[66:69]
	v_mfma_f32_16x16x32_f16 v[236:239], v[140:143], v[224:227], v[78:81]
	v_mfma_f32_16x16x32_f16 v[70:73], v[140:143], v[228:231], v[70:73]
	s_waitcnt vmcnt(13)
	v_mfma_f32_16x16x32_f16 v[140:143], v[152:155], v[94:97], v[188:191]
	v_mfma_f32_16x16x32_f16 v[74:77], v[152:155], v[180:183], v[74:77]
	v_mfma_f32_16x16x32_f16 v[82:85], v[152:155], v[224:227], v[82:85]
	v_mfma_f32_16x16x32_f16 v[62:65], v[152:155], v[228:231], v[62:65]
	s_waitcnt vmcnt(12)
	v_mfma_f32_16x16x32_f16 v[152:155], v[160:163], v[94:97], v[192:195]
	buffer_load_dwordx4 v[94:97], v147, s[16:19], s8 offen
	buffer_load_dwordx4 v[90:93], v148, s[16:19], s8 offen
	buffer_load_dwordx4 v[78:81], v149, s[16:19], s8 offen
	buffer_load_dwordx4 v[34:37], v150, s[16:19], s8 offen
	v_mfma_f32_16x16x32_f16 v[42:45], v[160:163], v[180:183], v[42:45]
	v_mfma_f32_16x16x32_f16 v[46:49], v[160:163], v[224:227], v[46:49]
	v_mfma_f32_16x16x32_f16 v[160:163], v[160:163], v[228:231], v[196:199]
	v_add_u32_e32 v100, s79, v100
	ds_read_b128 v[180:183], v100
	ds_read_b128 v[188:191], v100 offset:16384
	ds_read_b128 v[192:195], v100 offset:32768
	ds_read_b128 v[196:199], v100 offset:49152
	s_add_i32 s8, s22, s48
	s_waitcnt vmcnt(15) lgkmcnt(7)
	v_mfma_f32_16x16x32_f16 v[164:167], v[126:129], v[204:207], v[164:167]
	s_waitcnt lgkmcnt(6)
	v_mfma_f32_16x16x32_f16 v[168:171], v[126:129], v[208:211], v[168:171]
	s_waitcnt lgkmcnt(5)
	v_mfma_f32_16x16x32_f16 v[172:175], v[126:129], v[212:215], v[172:175]
	s_waitcnt lgkmcnt(4)
	v_mfma_f32_16x16x32_f16 v[86:89], v[126:129], v[216:219], v[86:89]
	s_waitcnt vmcnt(14)
	v_mfma_f32_16x16x32_f16 v[126:129], v[136:139], v[204:207], v[232:235]
	v_mfma_f32_16x16x32_f16 v[66:69], v[136:139], v[208:211], v[66:69]
	v_mfma_f32_16x16x32_f16 v[224:227], v[136:139], v[212:215], v[236:239]
	v_mfma_f32_16x16x32_f16 v[136:139], v[136:139], v[216:219], v[70:73]
	s_waitcnt vmcnt(13)
	v_mfma_f32_16x16x32_f16 v[140:143], v[184:187], v[204:207], v[140:143]
	v_mfma_f32_16x16x32_f16 v[74:77], v[184:187], v[208:211], v[74:77]
	v_mfma_f32_16x16x32_f16 v[228:231], v[184:187], v[212:215], v[82:85]
	v_mfma_f32_16x16x32_f16 v[184:187], v[184:187], v[216:219], v[62:65]
	s_waitcnt vmcnt(12)
	v_mfma_f32_16x16x32_f16 v[152:155], v[200:203], v[204:207], v[152:155]
	v_mfma_f32_16x16x32_f16 v[204:207], v[200:203], v[208:211], v[42:45]
	buffer_load_dwordx4 v[82:85], v147, s[16:19], s8 offen
	buffer_load_dwordx4 v[70:73], v148, s[16:19], s8 offen
	buffer_load_dwordx4 v[62:65], v149, s[16:19], s8 offen
	buffer_load_dwordx4 v[42:45], v150, s[16:19], s8 offen
	v_mfma_f32_16x16x32_f16 v[46:49], v[200:203], v[212:215], v[46:49]
	v_mfma_f32_16x16x32_f16 v[160:163], v[200:203], v[216:219], v[160:163]
	v_add_u32_e32 v0, 0x1ac00, v104
	ds_read_b128 v[240:243], v0
	ds_read_b128 v[244:247], v0 offset:16
	s_waitcnt vmcnt(12) lgkmcnt(5)
	v_mfma_f32_16x16x32_f16 v[164:167], v[122:125], v[180:183], v[164:167]
	v_mfma_f32_16x16x32_f16 v[126:129], v[156:159], v[180:183], v[126:129]
	v_mfma_f32_16x16x32_f16 v[140:143], v[176:179], v[180:183], v[140:143]
	v_mfma_f32_16x16x32_f16 v[152:155], v[220:223], v[180:183], v[152:155]
	s_waitcnt lgkmcnt(4)
	v_mfma_f32_16x16x32_f16 v[168:171], v[122:125], v[188:191], v[168:171]
	v_mfma_f32_16x16x32_f16 v[208:211], v[156:159], v[188:191], v[66:69]
	v_mfma_f32_16x16x32_f16 v[212:215], v[176:179], v[188:191], v[74:77]
	v_mfma_f32_16x16x32_f16 v[204:207], v[220:223], v[188:191], v[204:207]
	s_waitcnt lgkmcnt(3)
	v_mfma_f32_16x16x32_f16 v[172:175], v[122:125], v[192:195], v[172:175]
	v_cvt_pk_f16_f32 v232, v164, v165
	v_cvt_pk_f16_f32 v233, v166, v167
	v_pk_max_f16 v232, v232, 0
	v_pk_max_f16 v233, v233, 0
	v_mfma_f32_16x16x32_f16 v[224:227], v[156:159], v[192:195], v[224:227]
	v_cvt_pk_f16_f32 v234, v126, v127
	v_cvt_pk_f16_f32 v235, v128, v129
	v_pk_max_f16 v234, v234, 0
	v_pk_max_f16 v235, v235, 0
	v_mfma_f32_16x16x32_f16 v[228:231], v[176:179], v[192:195], v[228:231]
	v_cvt_pk_f16_f32 v236, v140, v141
	v_cvt_pk_f16_f32 v237, v142, v143
	v_pk_max_f16 v236, v236, 0
	v_pk_max_f16 v237, v237, 0
	v_mfma_f32_16x16x32_f16 v[216:219], v[220:223], v[192:195], v[46:49]
	v_cvt_pk_f16_f32 v238, v152, v153
	v_cvt_pk_f16_f32 v239, v154, v155
	v_pk_max_f16 v238, v238, 0
	v_pk_max_f16 v239, v239, 0
	s_waitcnt lgkmcnt(2)
	v_mfma_f32_16x16x32_f16 v[200:203], v[122:125], v[196:199], v[86:89]
	v_cvt_pk_f16_f32 v180, v168, v169
	v_cvt_pk_f16_f32 v181, v170, v171
	v_pk_max_f16 v180, v180, 0
	v_pk_max_f16 v181, v181, 0
	s_add_i32 s8, s22, s49
	buffer_load_dwordx4 v[86:89], v147, s[16:19], s8 offen
	buffer_load_dwordx4 v[74:77], v148, s[16:19], s8 offen
	buffer_load_dwordx4 v[66:69], v149, s[16:19], s8 offen
	buffer_load_dwordx4 v[46:49], v150, s[16:19], s8 offen
	v_mfma_f32_16x16x32_f16 v[136:139], v[156:159], v[196:199], v[136:139]
	v_cvt_pk_f16_f32 v182, v208, v209
	v_cvt_pk_f16_f32 v183, v210, v211
	v_pk_max_f16 v182, v182, 0
	v_pk_max_f16 v183, v183, 0
	s_waitcnt lgkmcnt(1)
	v_mfma_f32_16x16x32_f16 v[252:255], v[240:243], v[232:235], 0
	v_cvt_pk_f16_f32 v232, v172, v173
	v_cvt_pk_f16_f32 v233, v174, v175
	v_pk_max_f16 v232, v232, 0
	v_pk_max_f16 v233, v233, 0
	v_mfma_f32_16x16x32_f16 v[184:187], v[176:179], v[196:199], v[184:187]
	v_cvt_pk_f16_f32 v188, v212, v213
	v_cvt_pk_f16_f32 v189, v214, v215
	v_pk_max_f16 v188, v188, 0
	v_pk_max_f16 v189, v189, 0
	s_waitcnt lgkmcnt(0)
	v_mfma_f32_16x16x32_f16 v[252:255], v[244:247], v[236:239], v[252:255]
	ds_read_u16 v102, v114
	ds_read_u16 v103, v114 offset:512
	ds_read_u16 v115, v114 offset:1024
	ds_read_u16 v116, v114 offset:1536
	v_cvt_pk_f16_f32 v234, v224, v225
	v_cvt_pk_f16_f32 v235, v226, v227
	v_pk_max_f16 v234, v234, 0
	v_pk_max_f16 v235, v235, 0
	v_mfma_f32_16x16x32_f16 v[160:163], v[220:223], v[196:199], v[160:163]
	v_cvt_pk_f16_f32 v190, v204, v205
	v_cvt_pk_f16_f32 v191, v206, v207
	v_pk_max_f16 v190, v190, 0
	v_pk_max_f16 v191, v191, 0
	v_mfma_f32_16x16x32_f16 v[192:195], v[240:243], v[180:183], 0
	v_cvt_pk_f16_f32 v236, v228, v229
	v_cvt_pk_f16_f32 v237, v230, v231
	v_pk_max_f16 v236, v236, 0
	v_pk_max_f16 v237, v237, 0
	v_mfma_f32_16x16x32_f16 v[192:195], v[244:247], v[188:191], v[192:195]
	v_cvt_pk_f16_f32 v238, v216, v217
	v_cvt_pk_f16_f32 v239, v218, v219
	v_pk_max_f16 v238, v238, 0
	v_pk_max_f16 v239, v239, 0
	v_cvt_pk_f16_f32 v180, v200, v201
	v_cvt_pk_f16_f32 v181, v202, v203
	v_pk_max_f16 v180, v180, 0
	v_pk_max_f16 v181, v181, 0
	v_mfma_f32_16x16x32_f16 v[196:199], v[240:243], v[232:235], 0
	v_cvt_pk_f16_f32 v182, v136, v137
	v_cvt_pk_f16_f32 v183, v138, v139
	v_pk_max_f16 v182, v182, 0
	v_pk_max_f16 v183, v183, 0
	v_mfma_f32_16x16x32_f16 v[196:199], v[244:247], v[236:239], v[196:199]
	v_cvt_pk_f16_f32 v188, v184, v185
	v_cvt_pk_f16_f32 v189, v186, v187
	v_pk_max_f16 v188, v188, 0
	v_pk_max_f16 v189, v189, 0
	v_cvt_pk_f16_f32 v190, v160, v161
	v_cvt_pk_f16_f32 v191, v162, v163
	v_pk_max_f16 v190, v190, 0
	v_pk_max_f16 v191, v191, 0
	v_mfma_f32_16x16x32_f16 v[122:125], v[240:243], v[180:183], 0
	s_nop 0
	v_mfma_f32_16x16x32_f16 v[122:125], v[244:247], v[188:191], v[122:125]
	v_add_u32_e32 v145, 0x12c00, v105
	v_cndmask_b32_e64 v0, v252, v192, s[2:3]
	v_cndmask_b32_e64 v0, v0, v196, s[0:1]
	s_waitcnt vmcnt(16)
	v_cndmask_b32_e64 v1, v30, v134, s[0:1]
	v_bfi_b32 v30, s10, v1, v30
	v_perm_b32 v1, v22, v134, s24
	v_cndmask_b32_e64 v22, v22, v1, s[0:1]
	v_cndmask_b32_e64 v0, v0, v122, s[26:27]
	ds_write_b32 v112, v0
	v_bfi_b32 v1, s10, v135, v18
	v_perm_b32 v121, v10, v135, s24
	v_cndmask_b32_e64 v18, v18, v1, s[0:1]
	v_cndmask_b32_e64 v10, v10, v121, s[0:1]
	s_add_i32 s22, s22, 0x80000
	s_add_i32 s11, s11, 1
	s_mov_b64 s[86:87], -1
	s_add_u32 s12, s12, 4
	s_addc_u32 s13, s13, 0
	v_add_u32_e32 v104, 0x400, v104
	v_add_u32_e32 v105, 0x800, v105
	v_add_u32_e32 v114, 2, v114
	s_cmp_eq_u32 s22, 0x898000
	s_waitcnt lgkmcnt(0)
	s_barrier
	ds_read_b128 v[232:235], v113
	ds_read_b128 v[236:239], v113 offset:1024
	ds_read_b128 v[240:243], v145 offset:2048
	ds_read_b128 v[244:247], v145 offset:2064
	ds_read_b128 v[248:251], v145 offset:2080
	ds_read_b128 v[252:255], v145 offset:2096
	s_waitcnt lgkmcnt(5)
	v_add_f32_e32 v0, v232, v233
	v_add_f32_e32 v1, v234, v235
	v_add_f32_e32 v0, v0, v1
	v_add_f32_e32 v0, s30, v0
	s_waitcnt lgkmcnt(4)
	v_add_f32_e32 v121, v236, v237
	v_add_f32_e32 v144, v238, v239
	v_add_f32_e32 v121, v121, v144
	v_add_f32_e32 v0, v0, v121
	v_cvt_f16_f32_e32 v1, v0
	v_cvt_f16_f32_e32 v121, v0
	s_nop 1
	v_permlane16_swap_b32_e32 v1, v121
	s_cbranch_scc0 .LBB1_4
.LBB1_8:
	ds_write_b32 v106, v0
	s_waitcnt lgkmcnt(0)
	v_add_u32_e32 v0, 0x1ec00, v146
	s_barrier
	ds_read2st64_b32 v[0:1], v0 offset1:8
	s_lshl_b64 s[0:1], s[6:7], 2
	s_add_u32 s0, s14, s0
	s_addc_u32 s1, s15, s1
	s_waitcnt lgkmcnt(0)
	global_store_dword v146, v0, s[0:1]
	global_store_dword v146, v1, s[0:1] offset:2048
	s_endpgm
